# P8/P11 epilogues: counted residual-load waits together with the permlane-swap row sums
# baseline (speedup 1.0000x reference)
.LBB0_1121:
	s_lshl_b32 s4, s63, 8
	v_mov_b32_e32 v108, v0
	s_add_i32 s4, s4, s58
	v_and_b32_e32 v198, 64, v250
	v_and_or_b32 v216, v108, 15, s4
	s_lshl_b32 s4, s56, 8
	v_bfe_u32 v196, v108, 4, 2
	s_or_b32 s4, s4, s59
	v_lshl_or_b32 v214, v196, 3, s4
	v_ashrrev_i32_e32 v215, 31, v214
	v_ashrrev_i32_e32 v217, 31, v216
	v_lshlrev_b64 v[232:233], 1, v[214:215]
	v_lshl_add_u64 v[118:119], s[14:15], 0, v[232:233]
	v_lshlrev_b64 v[234:235], 11, v[216:217]
	v_lshl_add_u64 v[128:129], v[118:119], 0, v[234:235]
	global_load_dwordx4 v[192:195], v[128:129], off
	global_load_dwordx4 v[188:191], v[128:129], off offset:256
	v_or_b32_e32 v228, 16, v216
	v_ashrrev_i32_e32 v229, 31, v228
	v_or_b32_e32 v224, 32, v216
	v_ashrrev_i32_e32 v225, 31, v224
	v_or_b32_e32 v220, 48, v216
	v_lshlrev_b64 v[230:231], 11, v[228:229]
	v_ashrrev_i32_e32 v221, 31, v220
	v_lshl_add_u64 v[128:129], v[118:119], 0, v[230:231]
	v_lshlrev_b64 v[226:227], 11, v[224:225]
	v_add_u32_e32 v218, 0x80, v216
	v_add_u32_e32 v108, 0x90, v216
	global_load_dwordx4 v[184:187], v[128:129], off
	global_load_dwordx4 v[180:183], v[128:129], off offset:256
	v_lshl_add_u64 v[128:129], v[118:119], 0, v[226:227]
	v_lshlrev_b64 v[222:223], 11, v[220:221]
	v_ashrrev_i32_e32 v219, 31, v218
	v_ashrrev_i32_e32 v109, 31, v108
	global_load_dwordx4 v[176:179], v[128:129], off
	global_load_dwordx4 v[172:175], v[128:129], off offset:256
	v_lshl_add_u64 v[128:129], v[118:119], 0, v[222:223]
	v_add_u32_e32 v110, 0xa0, v216
	global_load_dwordx4 v[168:171], v[128:129], off
	global_load_dwordx4 v[164:167], v[128:129], off offset:256
	v_lshlrev_b64 v[128:129], 11, v[218:219]
	v_lshlrev_b64 v[108:109], 11, v[108:109]
	v_ashrrev_i32_e32 v111, 31, v110
	v_lshl_add_u64 v[128:129], v[118:119], 0, v[128:129]
	v_lshl_add_u64 v[108:109], v[118:119], 0, v[108:109]
	v_add_u32_e32 v116, 0xb0, v216
	global_load_dwordx4 v[160:163], v[128:129], off
	global_load_dwordx4 v[156:159], v[128:129], off offset:256
	global_load_dwordx4 v[152:155], v[108:109], off
	global_load_dwordx4 v[148:151], v[108:109], off offset:256
	v_lshlrev_b64 v[108:109], 11, v[110:111]
	v_ashrrev_i32_e32 v117, 31, v116
	v_lshl_add_u64 v[108:109], v[118:119], 0, v[108:109]
	global_load_dwordx4 v[136:139], v[108:109], off
	global_load_dwordx4 v[128:131], v[108:109], off offset:256
	v_lshlrev_b64 v[108:109], 11, v[116:117]
	v_lshl_add_u64 v[108:109], v[118:119], 0, v[108:109]
	global_load_dwordx4 v[116:119], v[108:109], off
	s_nop 0
	global_load_dwordx4 v[108:111], v[108:109], off offset:256
	v_xor_b32_e32 v197, 16, v250
	v_add_u32_e32 v198, 64, v198
	v_cmp_lt_i32_e32 vcc, v197, v198
	s_lshl_b32 s44, s56, 2
	s_ashr_i32 s45, s44, 31
	v_cndmask_b32_e32 v197, v250, v197, vcc
	v_lshlrev_b32_e32 v237, 2, v197
	v_xor_b32_e32 v197, 32, v250
	v_cmp_lt_i32_e32 vcc, v197, v198
	s_waitcnt vmcnt(15)
	v_lshlrev_b32_e32 v198, 16, v194
	v_cndmask_b32_e32 v197, v250, v197, vcc
	v_lshlrev_b32_e32 v238, 2, v197
	v_cmp_eq_u32_e32 vcc, 0, v196
	v_lshlrev_b32_e32 v196, 16, v192
	v_and_b32_e32 v197, 0xffff0000, v192
	v_lshlrev_b32_e32 v192, 16, v193
	v_and_b32_e32 v193, 0xffff0000, v193
	v_and_b32_e32 v199, 0xffff0000, v194
	v_lshlrev_b32_e32 v194, 16, v195
	v_and_b32_e32 v195, 0xffff0000, v195
	v_pk_add_f32 v[144:145], v[144:145], v[196:197]
	v_pk_add_f32 v[146:147], v[146:147], v[192:193]
	v_pk_add_f32 v[192:193], v[142:143], v[194:195]
	v_pk_add_f32 v[142:143], v[140:141], v[198:199]
	v_cvt_pk_bf16_f32 v140, v144, v145
	v_lshl_add_u64 v[144:145], s[14:15], 0, v[234:235]
	v_cvt_pk_bf16_f32 v141, v146, v147
	v_cvt_pk_bf16_f32 v142, v142, v143
	v_cvt_pk_bf16_f32 v143, v192, v193
	v_lshl_add_u64 v[144:145], v[144:145], 0, v[232:233]
	global_store_dwordx4 v[144:145], v[140:143], off
	v_lshlrev_b32_e32 v146, 16, v140
	v_lshlrev_b32_e32 v147, 16, v141
	v_and_b32_e32 v140, 0xffff0000, v140
	v_and_b32_e32 v141, 0xffff0000, v141
	v_mul_f32_e32 v140, v140, v140
	v_mul_f32_e32 v141, v141, v141
	v_lshlrev_b32_e32 v192, 16, v142
	v_and_b32_e32 v142, 0xffff0000, v142
	v_lshlrev_b32_e32 v193, 16, v143
	v_and_b32_e32 v143, 0xffff0000, v143
	v_fmac_f32_e32 v140, v146, v146
	v_fmac_f32_e32 v141, v147, v147
	v_add_f32_e32 v140, v140, v141
	v_mul_f32_e32 v141, v142, v142
	v_mul_f32_e32 v142, v143, v143
	v_fmac_f32_e32 v141, v192, v192
	v_fmac_f32_e32 v142, v193, v193
	v_add_f32_e32 v141, v141, v142
	v_add_f32_e32 v192, v140, v141
	s_waitcnt vmcnt(15)
	v_lshlrev_b32_e32 v140, 16, v188
	v_and_b32_e32 v141, 0xffff0000, v188
	v_lshlrev_b32_e32 v142, 16, v189
	v_and_b32_e32 v143, 0xffff0000, v189
	v_lshlrev_b32_e32 v146, 16, v190
	v_and_b32_e32 v147, 0xffff0000, v190
	v_lshlrev_b32_e32 v188, 16, v191
	v_and_b32_e32 v189, 0xffff0000, v191
	v_pk_add_f32 v[134:135], v[134:135], v[142:143]
	v_pk_add_f32 v[132:133], v[132:133], v[140:141]
	v_pk_add_f32 v[140:141], v[126:127], v[188:189]
	v_pk_add_f32 v[126:127], v[124:125], v[146:147]
	v_cvt_pk_bf16_f32 v124, v132, v133
	v_cvt_pk_bf16_f32 v125, v134, v135
	v_cvt_pk_bf16_f32 v126, v126, v127
	v_cvt_pk_bf16_f32 v127, v140, v141
	global_store_dwordx4 v[144:145], v[124:127], off offset:256
	v_lshlrev_b32_e32 v132, 16, v124
	v_lshlrev_b32_e32 v133, 16, v125
	v_and_b32_e32 v124, 0xffff0000, v124
	v_and_b32_e32 v125, 0xffff0000, v125
	v_mul_f32_e32 v124, v124, v124
	v_mul_f32_e32 v125, v125, v125
	v_lshlrev_b32_e32 v134, 16, v126
	v_and_b32_e32 v126, 0xffff0000, v126
	v_lshlrev_b32_e32 v135, 16, v127
	v_and_b32_e32 v127, 0xffff0000, v127
	v_fmac_f32_e32 v124, v132, v132
	v_fmac_f32_e32 v125, v133, v133
	v_add_f32_e32 v124, v124, v125
	v_mul_f32_e32 v125, v126, v126
	v_mul_f32_e32 v126, v127, v127
	v_fmac_f32_e32 v125, v134, v134
	v_fmac_f32_e32 v126, v135, v135
	v_add_f32_e32 v125, v125, v126
	v_add_f32_e32 v124, v124, v125
	v_add_f32_e32 v124, v192, v124
	v_mov_b32_e32 v125, v124
	s_nop 3
	v_permlane16_swap_b32_e32 v124, v125
	s_nop 1
	s_waitcnt lgkmcnt(0)
	v_add_f32_e32 v124, v124, v125
	v_mov_b32_e32 v125, v124
	s_nop 3
	v_permlane32_swap_b32_e32 v124, v125
	s_nop 1
	s_and_saveexec_b64 s[4:5], vcc
	s_cbranch_execz .LBB0_1123
	v_lshlrev_b64 v[126:127], 6, v[216:217]
	v_lshl_add_u64 v[126:127], s[18:19], 0, v[126:127]
	v_lshl_add_u64 v[126:127], s[44:45], 2, v[126:127]
	s_lshl_b32 s56, s53, 2
	v_lshl_add_u64 v[126:127], v[126:127], 0, s[56:57]
	s_waitcnt lgkmcnt(0)
	v_add_f32_e32 v124, v124, v125
	global_store_dword v[126:127], v124, off
.LBB0_1123:
	s_or_b64 exec, exec, s[4:5]
	s_waitcnt vmcnt(15)
	v_lshlrev_b32_e32 v124, 16, v184
	s_waitcnt lgkmcnt(0)
	v_and_b32_e32 v125, 0xffff0000, v184
	v_lshlrev_b32_e32 v126, 16, v185
	v_and_b32_e32 v127, 0xffff0000, v185
	v_lshlrev_b32_e32 v132, 16, v186
	v_and_b32_e32 v133, 0xffff0000, v186
	v_lshlrev_b32_e32 v134, 16, v187
	v_and_b32_e32 v135, 0xffff0000, v187
	v_pk_add_f32 v[120:121], v[120:121], v[124:125]
	v_pk_add_f32 v[122:123], v[122:123], v[126:127]
	v_pk_add_f32 v[124:125], v[114:115], v[134:135]
	v_pk_add_f32 v[114:115], v[112:113], v[132:133]
	v_cvt_pk_bf16_f32 v112, v120, v121
	v_cvt_pk_bf16_f32 v113, v122, v123
	v_and_b32_e32 v121, 0xffff0000, v112
	v_lshlrev_b32_e32 v120, 16, v112
	v_and_b32_e32 v123, 0xffff0000, v113
	v_mul_f32_e32 v121, v121, v121
	v_cvt_pk_bf16_f32 v114, v114, v115
	v_cvt_pk_bf16_f32 v115, v124, v125
	v_lshlrev_b32_e32 v122, 16, v113
	v_fmac_f32_e32 v121, v120, v120
	v_mul_f32_e32 v120, v123, v123
	v_and_b32_e32 v125, 0xffff0000, v114
	v_and_b32_e32 v127, 0xffff0000, v115
	v_fmac_f32_e32 v120, v122, v122
	v_lshlrev_b32_e32 v124, 16, v114
	v_lshlrev_b32_e32 v126, 16, v115
	v_add_f32_e32 v120, v121, v120
	v_mul_f32_e32 v121, v125, v125
	v_mul_f32_e32 v122, v127, v127
	v_fmac_f32_e32 v121, v124, v124
	v_fmac_f32_e32 v122, v126, v126
	v_add_f32_e32 v121, v121, v122
	v_add_f32_e32 v132, v120, v121
	s_waitcnt vmcnt(14)
	v_lshlrev_b32_e32 v120, 16, v180
	v_and_b32_e32 v121, 0xffff0000, v180
	v_lshlrev_b32_e32 v122, 16, v181
	v_and_b32_e32 v123, 0xffff0000, v181
	v_lshlrev_b32_e32 v124, 16, v182
	v_and_b32_e32 v125, 0xffff0000, v182
	v_lshlrev_b32_e32 v126, 16, v183
	v_and_b32_e32 v127, 0xffff0000, v183
	v_pk_add_f32 v[104:105], v[104:105], v[120:121]
	v_pk_add_f32 v[106:107], v[106:107], v[122:123]
	v_pk_add_f32 v[120:121], v[102:103], v[126:127]
	v_pk_add_f32 v[100:101], v[100:101], v[124:125]
	v_cvt_pk_bf16_f32 v102, v104, v105
	v_cvt_pk_bf16_f32 v103, v106, v107
	v_cvt_pk_bf16_f32 v104, v100, v101
	v_and_b32_e32 v101, 0xffff0000, v102
	v_lshlrev_b32_e32 v100, 16, v102
	v_and_b32_e32 v107, 0xffff0000, v103
	v_mul_f32_e32 v101, v101, v101
	v_cvt_pk_bf16_f32 v105, v120, v121
	v_lshlrev_b32_e32 v106, 16, v103
	v_fmac_f32_e32 v101, v100, v100
	v_mul_f32_e32 v100, v107, v107
	v_and_b32_e32 v121, 0xffff0000, v104
	v_and_b32_e32 v123, 0xffff0000, v105
	v_fmac_f32_e32 v100, v106, v106
	v_lshlrev_b32_e32 v120, 16, v104
	v_lshlrev_b32_e32 v122, 16, v105
	v_add_f32_e32 v100, v101, v100
	v_mul_f32_e32 v101, v121, v121
	v_mul_f32_e32 v106, v123, v123
	v_fmac_f32_e32 v101, v120, v120
	v_fmac_f32_e32 v106, v122, v122
	v_add_f32_e32 v101, v101, v106
	v_add_f32_e32 v100, v100, v101
	v_add_f32_e32 v100, v132, v100
	v_mov_b32_e32 v101, v100
	s_nop 3
	v_permlane16_swap_b32_e32 v100, v101
	s_nop 1
	v_lshl_add_u64 v[106:107], s[14:15], 0, v[230:231]
	v_lshl_add_u64 v[106:107], v[214:215], 1, v[106:107]
	global_store_dwordx4 v[106:107], v[112:115], off
	global_store_dwordx4 v[106:107], v[102:105], off offset:256
	s_waitcnt lgkmcnt(0)
	v_add_f32_e32 v100, v100, v101
	v_mov_b32_e32 v101, v100
	s_nop 3
	v_permlane32_swap_b32_e32 v100, v101
	s_nop 1
	s_and_saveexec_b64 s[4:5], vcc
	s_cbranch_execz .LBB0_1125
	v_lshlrev_b64 v[102:103], 6, v[228:229]
	v_lshl_add_u64 v[102:103], s[18:19], 0, v[102:103]
	v_lshl_add_u64 v[102:103], s[44:45], 2, v[102:103]
	s_lshl_b32 s56, s53, 2
	v_lshl_add_u64 v[102:103], v[102:103], 0, s[56:57]
	s_waitcnt lgkmcnt(0)
	v_add_f32_e32 v100, v100, v101
	global_store_dword v[102:103], v100, off
.LBB0_1125:
	s_or_b64 exec, exec, s[4:5]
	s_waitcnt vmcnt(15)
	v_lshlrev_b32_e32 v100, 16, v176
	s_waitcnt lgkmcnt(0)
	v_and_b32_e32 v101, 0xffff0000, v176
	v_lshlrev_b32_e32 v102, 16, v177
	v_and_b32_e32 v103, 0xffff0000, v177
	v_lshlrev_b32_e32 v104, 16, v178
	v_and_b32_e32 v105, 0xffff0000, v178
	v_lshlrev_b32_e32 v106, 16, v179
	v_and_b32_e32 v107, 0xffff0000, v179
	v_pk_add_f32 v[96:97], v[96:97], v[100:101]
	v_pk_add_f32 v[98:99], v[98:99], v[102:103]
	v_pk_add_f32 v[100:101], v[94:95], v[106:107]
	v_pk_add_f32 v[94:95], v[92:93], v[104:105]
	v_cvt_pk_bf16_f32 v92, v96, v97
	v_cvt_pk_bf16_f32 v93, v98, v99
	v_and_b32_e32 v97, 0xffff0000, v92
	v_lshlrev_b32_e32 v96, 16, v92
	v_and_b32_e32 v99, 0xffff0000, v93
	v_mul_f32_e32 v97, v97, v97
	v_cvt_pk_bf16_f32 v94, v94, v95
	v_cvt_pk_bf16_f32 v95, v100, v101
	v_lshlrev_b32_e32 v98, 16, v93
	v_fmac_f32_e32 v97, v96, v96
	v_mul_f32_e32 v96, v99, v99
	v_and_b32_e32 v101, 0xffff0000, v94
	v_and_b32_e32 v103, 0xffff0000, v95
	v_fmac_f32_e32 v96, v98, v98
	v_lshlrev_b32_e32 v100, 16, v94
	v_lshlrev_b32_e32 v102, 16, v95
	v_add_f32_e32 v96, v97, v96
	v_mul_f32_e32 v97, v101, v101
	v_mul_f32_e32 v98, v103, v103
	v_fmac_f32_e32 v97, v100, v100
	v_fmac_f32_e32 v98, v102, v102
	v_add_f32_e32 v97, v97, v98
	v_add_f32_e32 v104, v96, v97
	s_waitcnt vmcnt(14)
	v_lshlrev_b32_e32 v96, 16, v172
	v_and_b32_e32 v97, 0xffff0000, v172
	v_lshlrev_b32_e32 v98, 16, v173
	v_and_b32_e32 v99, 0xffff0000, v173
	v_lshlrev_b32_e32 v100, 16, v174
	v_and_b32_e32 v101, 0xffff0000, v174
	v_lshlrev_b32_e32 v102, 16, v175
	v_and_b32_e32 v103, 0xffff0000, v175
	v_pk_add_f32 v[88:89], v[88:89], v[96:97]
	v_pk_add_f32 v[90:91], v[90:91], v[98:99]
	v_pk_add_f32 v[96:97], v[86:87], v[102:103]
	v_pk_add_f32 v[84:85], v[84:85], v[100:101]
	v_cvt_pk_bf16_f32 v86, v88, v89
	v_cvt_pk_bf16_f32 v87, v90, v91
	v_cvt_pk_bf16_f32 v88, v84, v85
	v_and_b32_e32 v85, 0xffff0000, v86
	v_lshlrev_b32_e32 v84, 16, v86
	v_and_b32_e32 v91, 0xffff0000, v87
	v_mul_f32_e32 v85, v85, v85
	v_cvt_pk_bf16_f32 v89, v96, v97
	v_lshlrev_b32_e32 v90, 16, v87
	v_fmac_f32_e32 v85, v84, v84
	v_mul_f32_e32 v84, v91, v91
	v_and_b32_e32 v97, 0xffff0000, v88
	v_and_b32_e32 v99, 0xffff0000, v89
	v_fmac_f32_e32 v84, v90, v90
	v_lshlrev_b32_e32 v96, 16, v88
	v_lshlrev_b32_e32 v98, 16, v89
	v_add_f32_e32 v84, v85, v84
	v_mul_f32_e32 v85, v97, v97
	v_mul_f32_e32 v90, v99, v99
	v_fmac_f32_e32 v85, v96, v96
	v_fmac_f32_e32 v90, v98, v98
	v_add_f32_e32 v85, v85, v90
	v_add_f32_e32 v84, v84, v85
	v_add_f32_e32 v84, v104, v84
	v_mov_b32_e32 v85, v84
	s_nop 3
	v_permlane16_swap_b32_e32 v84, v85
	s_nop 1
	v_lshl_add_u64 v[90:91], s[14:15], 0, v[226:227]
	v_lshl_add_u64 v[90:91], v[214:215], 1, v[90:91]
	global_store_dwordx4 v[90:91], v[92:95], off
	global_store_dwordx4 v[90:91], v[86:89], off offset:256
	s_waitcnt lgkmcnt(0)
	v_add_f32_e32 v84, v84, v85
	v_mov_b32_e32 v85, v84
	s_nop 3
	v_permlane32_swap_b32_e32 v84, v85
	s_nop 1
	s_and_saveexec_b64 s[4:5], vcc
	s_mov_b32 s76, 0xe000
	s_movk_i32 s75, 0x3400
	v_readlane_b32 s74, v255, 38
	s_cbranch_execz .LBB0_1127
	v_lshlrev_b64 v[86:87], 6, v[224:225]
	v_lshl_add_u64 v[86:87], s[18:19], 0, v[86:87]
	v_lshl_add_u64 v[86:87], s[44:45], 2, v[86:87]
	s_lshl_b32 s56, s53, 2
	v_lshl_add_u64 v[86:87], v[86:87], 0, s[56:57]
	s_waitcnt lgkmcnt(0)
	v_add_f32_e32 v84, v84, v85
	global_store_dword v[86:87], v84, off
.LBB0_1127:
	s_or_b64 exec, exec, s[4:5]
	s_waitcnt vmcnt(15)
	v_lshlrev_b32_e32 v84, 16, v168
	s_waitcnt lgkmcnt(0)
	v_and_b32_e32 v85, 0xffff0000, v168
	v_lshlrev_b32_e32 v86, 16, v169
	v_and_b32_e32 v87, 0xffff0000, v169
	v_lshlrev_b32_e32 v88, 16, v170
	v_and_b32_e32 v89, 0xffff0000, v170
	v_lshlrev_b32_e32 v90, 16, v171
	v_and_b32_e32 v91, 0xffff0000, v171
	v_pk_add_f32 v[80:81], v[80:81], v[84:85]
	v_pk_add_f32 v[82:83], v[82:83], v[86:87]
	v_pk_add_f32 v[84:85], v[78:79], v[90:91]
	v_pk_add_f32 v[78:79], v[76:77], v[88:89]
	v_cvt_pk_bf16_f32 v76, v80, v81
	v_cvt_pk_bf16_f32 v77, v82, v83
	v_and_b32_e32 v81, 0xffff0000, v76
	v_lshlrev_b32_e32 v80, 16, v76
	v_and_b32_e32 v83, 0xffff0000, v77
	v_mul_f32_e32 v81, v81, v81
	v_cvt_pk_bf16_f32 v78, v78, v79
	v_cvt_pk_bf16_f32 v79, v84, v85
	v_lshlrev_b32_e32 v82, 16, v77
	v_fmac_f32_e32 v81, v80, v80
	v_mul_f32_e32 v80, v83, v83
	v_and_b32_e32 v85, 0xffff0000, v78
	v_and_b32_e32 v87, 0xffff0000, v79
	v_fmac_f32_e32 v80, v82, v82
	v_lshlrev_b32_e32 v84, 16, v78
	v_lshlrev_b32_e32 v86, 16, v79
	v_add_f32_e32 v80, v81, v80
	v_mul_f32_e32 v81, v85, v85
	v_mul_f32_e32 v82, v87, v87
	v_fmac_f32_e32 v81, v84, v84
	v_fmac_f32_e32 v82, v86, v86
	v_add_f32_e32 v81, v81, v82
	v_add_f32_e32 v88, v80, v81
	s_waitcnt vmcnt(14)
	v_lshlrev_b32_e32 v80, 16, v164
	v_and_b32_e32 v81, 0xffff0000, v164
	v_lshlrev_b32_e32 v82, 16, v165
	v_and_b32_e32 v83, 0xffff0000, v165
	v_lshlrev_b32_e32 v84, 16, v166
	v_and_b32_e32 v85, 0xffff0000, v166
	v_lshlrev_b32_e32 v86, 16, v167
	v_and_b32_e32 v87, 0xffff0000, v167
	v_pk_add_f32 v[72:73], v[72:73], v[80:81]
	v_pk_add_f32 v[74:75], v[74:75], v[82:83]
	v_pk_add_f32 v[80:81], v[70:71], v[86:87]
	v_pk_add_f32 v[68:69], v[68:69], v[84:85]
	v_cvt_pk_bf16_f32 v70, v72, v73
	v_cvt_pk_bf16_f32 v71, v74, v75
	v_cvt_pk_bf16_f32 v72, v68, v69
	v_and_b32_e32 v69, 0xffff0000, v70
	v_lshlrev_b32_e32 v68, 16, v70
	v_and_b32_e32 v75, 0xffff0000, v71
	v_mul_f32_e32 v69, v69, v69
	v_cvt_pk_bf16_f32 v73, v80, v81
	v_lshlrev_b32_e32 v74, 16, v71
	v_fmac_f32_e32 v69, v68, v68
	v_mul_f32_e32 v68, v75, v75
	v_and_b32_e32 v81, 0xffff0000, v72
	v_and_b32_e32 v83, 0xffff0000, v73
	v_fmac_f32_e32 v68, v74, v74
	v_lshlrev_b32_e32 v80, 16, v72
	v_lshlrev_b32_e32 v82, 16, v73
	v_add_f32_e32 v68, v69, v68
	v_mul_f32_e32 v69, v81, v81
	v_mul_f32_e32 v74, v83, v83
	v_fmac_f32_e32 v69, v80, v80
	v_fmac_f32_e32 v74, v82, v82
	v_add_f32_e32 v69, v69, v74
	v_add_f32_e32 v68, v68, v69
	v_add_f32_e32 v68, v88, v68
	v_mov_b32_e32 v69, v68
	s_nop 3
	v_permlane16_swap_b32_e32 v68, v69
	s_nop 1
	v_lshl_add_u64 v[74:75], s[14:15], 0, v[222:223]
	v_lshl_add_u64 v[74:75], v[214:215], 1, v[74:75]
	global_store_dwordx4 v[74:75], v[76:79], off
	global_store_dwordx4 v[74:75], v[70:73], off offset:256
	s_waitcnt lgkmcnt(0)
	v_add_f32_e32 v68, v68, v69
	v_mov_b32_e32 v69, v68
	s_nop 3
	v_permlane32_swap_b32_e32 v68, v69
	s_nop 1
	s_and_saveexec_b64 s[4:5], vcc
	s_cbranch_execz .LBB0_1129
	v_lshlrev_b64 v[70:71], 6, v[220:221]
	v_lshl_add_u64 v[70:71], s[18:19], 0, v[70:71]
	v_lshl_add_u64 v[70:71], s[44:45], 2, v[70:71]
	s_lshl_b32 s56, s53, 2
	v_lshl_add_u64 v[70:71], v[70:71], 0, s[56:57]
	s_waitcnt lgkmcnt(0)
	v_add_f32_e32 v68, v68, v69
	global_store_dword v[70:71], v68, off
.LBB0_1129:
	s_or_b64 exec, exec, s[4:5]
	s_waitcnt vmcnt(15)
	v_lshlrev_b32_e32 v68, 16, v160
	s_waitcnt lgkmcnt(0)
	v_and_b32_e32 v69, 0xffff0000, v160
	v_lshlrev_b32_e32 v70, 16, v161
	v_and_b32_e32 v71, 0xffff0000, v161
	v_lshlrev_b32_e32 v72, 16, v162
	v_and_b32_e32 v73, 0xffff0000, v162
	v_lshlrev_b32_e32 v74, 16, v163
	v_and_b32_e32 v75, 0xffff0000, v163
	v_pk_add_f32 v[64:65], v[64:65], v[68:69]
	v_pk_add_f32 v[66:67], v[66:67], v[70:71]
	v_pk_add_f32 v[68:69], v[62:63], v[74:75]
	v_pk_add_f32 v[62:63], v[60:61], v[72:73]
	v_cvt_pk_bf16_f32 v60, v64, v65
	v_cvt_pk_bf16_f32 v61, v66, v67
	v_and_b32_e32 v65, 0xffff0000, v60
	v_lshlrev_b32_e32 v64, 16, v60
	v_and_b32_e32 v67, 0xffff0000, v61
	v_mul_f32_e32 v65, v65, v65
	v_cvt_pk_bf16_f32 v62, v62, v63
	v_cvt_pk_bf16_f32 v63, v68, v69
	v_lshlrev_b32_e32 v66, 16, v61
	v_fmac_f32_e32 v65, v64, v64
	v_mul_f32_e32 v64, v67, v67
	v_and_b32_e32 v69, 0xffff0000, v62
	v_and_b32_e32 v71, 0xffff0000, v63
	v_fmac_f32_e32 v64, v66, v66
	v_lshlrev_b32_e32 v68, 16, v62
	v_lshlrev_b32_e32 v70, 16, v63
	v_add_f32_e32 v64, v65, v64
	v_mul_f32_e32 v65, v69, v69
	v_mul_f32_e32 v66, v71, v71
	v_fmac_f32_e32 v65, v68, v68
	v_fmac_f32_e32 v66, v70, v70
	v_add_f32_e32 v65, v65, v66
	v_add_f32_e32 v72, v64, v65
	s_waitcnt vmcnt(14)
	v_lshlrev_b32_e32 v64, 16, v156
	v_and_b32_e32 v65, 0xffff0000, v156
	v_lshlrev_b32_e32 v66, 16, v157
	v_and_b32_e32 v67, 0xffff0000, v157
	v_lshlrev_b32_e32 v68, 16, v158
	v_and_b32_e32 v69, 0xffff0000, v158
	v_lshlrev_b32_e32 v70, 16, v159
	v_and_b32_e32 v71, 0xffff0000, v159
	v_pk_add_f32 v[56:57], v[56:57], v[64:65]
	v_pk_add_f32 v[58:59], v[58:59], v[66:67]
	v_pk_add_f32 v[64:65], v[54:55], v[70:71]
	v_pk_add_f32 v[52:53], v[52:53], v[68:69]
	v_cvt_pk_bf16_f32 v54, v56, v57
	v_cvt_pk_bf16_f32 v55, v58, v59
	v_cvt_pk_bf16_f32 v56, v52, v53
	v_and_b32_e32 v53, 0xffff0000, v54
	v_lshlrev_b32_e32 v52, 16, v54
	v_and_b32_e32 v59, 0xffff0000, v55
	v_mul_f32_e32 v53, v53, v53
	v_cvt_pk_bf16_f32 v57, v64, v65
	v_lshlrev_b32_e32 v58, 16, v55
	v_fmac_f32_e32 v53, v52, v52
	v_mul_f32_e32 v52, v59, v59
	v_and_b32_e32 v65, 0xffff0000, v56
	v_and_b32_e32 v67, 0xffff0000, v57
	v_fmac_f32_e32 v52, v58, v58
	v_lshlrev_b32_e32 v64, 16, v56
	v_lshlrev_b32_e32 v66, 16, v57
	v_add_f32_e32 v52, v53, v52
	v_mul_f32_e32 v53, v65, v65
	v_mul_f32_e32 v58, v67, v67
	v_fmac_f32_e32 v53, v64, v64
	v_fmac_f32_e32 v58, v66, v66
	v_add_f32_e32 v53, v53, v58
	v_add_f32_e32 v52, v52, v53
	v_add_f32_e32 v52, v72, v52
	v_mov_b32_e32 v53, v52
	s_nop 3
	v_permlane16_swap_b32_e32 v52, v53
	s_nop 1
	v_lshlrev_b64 v[58:59], 10, v[218:219]
	v_lshl_add_u64 v[58:59], v[58:59], 1, s[14:15]
	v_lshl_add_u64 v[58:59], v[214:215], 1, v[58:59]
	global_store_dwordx4 v[58:59], v[60:63], off
	global_store_dwordx4 v[58:59], v[54:57], off offset:256
	s_waitcnt lgkmcnt(0)
	v_add_f32_e32 v52, v52, v53
	v_mov_b32_e32 v53, v52
	s_nop 3
	v_permlane32_swap_b32_e32 v52, v53
	s_nop 1
	s_and_saveexec_b64 s[4:5], vcc
	s_cbranch_execz .LBB0_1131
	v_lshlrev_b64 v[54:55], 6, v[218:219]
	v_lshl_add_u64 v[54:55], s[18:19], 0, v[54:55]
	v_lshl_add_u64 v[54:55], s[44:45], 2, v[54:55]
	s_lshl_b32 s56, s53, 2
	v_lshl_add_u64 v[54:55], v[54:55], 0, s[56:57]
	s_waitcnt lgkmcnt(0)
	v_add_f32_e32 v52, v52, v53
	global_store_dword v[54:55], v52, off
.LBB0_1131:
	s_or_b64 exec, exec, s[4:5]
	s_waitcnt vmcnt(15)
	v_lshlrev_b32_e32 v52, 16, v152
	s_waitcnt lgkmcnt(0)
	v_and_b32_e32 v53, 0xffff0000, v152
	v_lshlrev_b32_e32 v54, 16, v153
	v_and_b32_e32 v55, 0xffff0000, v153
	v_lshlrev_b32_e32 v56, 16, v154
	v_and_b32_e32 v57, 0xffff0000, v154
	v_lshlrev_b32_e32 v58, 16, v155
	v_and_b32_e32 v59, 0xffff0000, v155
	v_pk_add_f32 v[48:49], v[48:49], v[52:53]
	v_pk_add_f32 v[50:51], v[50:51], v[54:55]
	v_pk_add_f32 v[52:53], v[46:47], v[58:59]
	v_pk_add_f32 v[46:47], v[44:45], v[56:57]
	v_cvt_pk_bf16_f32 v44, v48, v49
	v_cvt_pk_bf16_f32 v45, v50, v51
	v_and_b32_e32 v49, 0xffff0000, v44
	v_lshlrev_b32_e32 v48, 16, v44
	v_and_b32_e32 v51, 0xffff0000, v45
	v_mul_f32_e32 v49, v49, v49
	v_cvt_pk_bf16_f32 v46, v46, v47
	v_cvt_pk_bf16_f32 v47, v52, v53
	v_lshlrev_b32_e32 v50, 16, v45
	v_fmac_f32_e32 v49, v48, v48
	v_mul_f32_e32 v48, v51, v51
	v_and_b32_e32 v53, 0xffff0000, v46
	v_and_b32_e32 v55, 0xffff0000, v47
	v_fmac_f32_e32 v48, v50, v50
	v_lshlrev_b32_e32 v52, 16, v46
	v_lshlrev_b32_e32 v54, 16, v47
	v_add_f32_e32 v48, v49, v48
	v_mul_f32_e32 v49, v53, v53
	v_mul_f32_e32 v50, v55, v55
	v_fmac_f32_e32 v49, v52, v52
	v_fmac_f32_e32 v50, v54, v54
	v_add_f32_e32 v49, v49, v50
	v_add_f32_e32 v56, v48, v49
	s_waitcnt vmcnt(14)
	v_lshlrev_b32_e32 v48, 16, v148
	v_and_b32_e32 v49, 0xffff0000, v148
	v_lshlrev_b32_e32 v50, 16, v149
	v_and_b32_e32 v51, 0xffff0000, v149
	v_lshlrev_b32_e32 v52, 16, v150
	v_and_b32_e32 v53, 0xffff0000, v150
	v_pk_add_f32 v[40:41], v[40:41], v[48:49]
	v_lshlrev_b32_e32 v54, 16, v151
	v_and_b32_e32 v55, 0xffff0000, v151
	v_pk_add_f32 v[42:43], v[42:43], v[50:51]
	v_pk_add_f32 v[36:37], v[36:37], v[52:53]
	v_cvt_pk_bf16_f32 v40, v40, v41
	v_pk_add_f32 v[38:39], v[38:39], v[54:55]
	v_cvt_pk_bf16_f32 v41, v42, v43
	v_cvt_pk_bf16_f32 v42, v36, v37
	v_and_b32_e32 v37, 0xffff0000, v40
	v_cvt_pk_bf16_f32 v43, v38, v39
	v_lshlrev_b32_e32 v36, 16, v40
	v_and_b32_e32 v39, 0xffff0000, v41
	v_mul_f32_e32 v37, v37, v37
	v_lshlrev_b32_e32 v38, 16, v41
	v_fmac_f32_e32 v37, v36, v36
	v_mul_f32_e32 v36, v39, v39
	v_and_b32_e32 v49, 0xffff0000, v42
	v_and_b32_e32 v51, 0xffff0000, v43
	v_fmac_f32_e32 v36, v38, v38
	v_lshlrev_b32_e32 v48, 16, v42
	v_lshlrev_b32_e32 v50, 16, v43
	v_add_f32_e32 v36, v37, v36
	v_mul_f32_e32 v37, v49, v49
	v_mul_f32_e32 v38, v51, v51
	v_fmac_f32_e32 v37, v48, v48
	v_fmac_f32_e32 v38, v50, v50
	v_add_f32_e32 v37, v37, v38
	v_add_f32_e32 v36, v36, v37
	v_add_f32_e32 v38, v56, v36
	v_mov_b32_e32 v39, v38
	s_nop 3
	v_permlane16_swap_b32_e32 v38, v39
	s_nop 1
	v_add_u32_e32 v36, 0x90, v216
	v_ashrrev_i32_e32 v37, 31, v36
	v_lshlrev_b64 v[48:49], 11, v[36:37]
	v_lshl_add_u64 v[48:49], s[14:15], 0, v[48:49]
	s_waitcnt lgkmcnt(0)
	v_add_f32_e32 v38, v38, v39
	v_mov_b32_e32 v39, v38
	s_nop 3
	v_permlane32_swap_b32_e32 v38, v39
	s_nop 1
	v_lshl_add_u64 v[48:49], v[214:215], 1, v[48:49]
	global_store_dwordx4 v[48:49], v[44:47], off
	global_store_dwordx4 v[48:49], v[40:43], off offset:256
	s_and_saveexec_b64 s[4:5], vcc
	s_cbranch_execz .LBB0_1133
	v_lshlrev_b64 v[36:37], 6, v[36:37]
	v_lshl_add_u64 v[36:37], s[18:19], 0, v[36:37]
	v_lshl_add_u64 v[36:37], s[44:45], 2, v[36:37]
	s_lshl_b32 s56, s53, 2
	v_lshl_add_u64 v[36:37], v[36:37], 0, s[56:57]
	s_waitcnt lgkmcnt(0)
	v_add_f32_e32 v38, v38, v39
	global_store_dword v[36:37], v38, off
.LBB0_1133:
	s_or_b64 exec, exec, s[4:5]
	s_waitcnt vmcnt(15)
	v_lshlrev_b32_e32 v36, 16, v136
	v_and_b32_e32 v37, 0xffff0000, v136
	v_lshlrev_b32_e32 v38, 16, v137
	s_waitcnt lgkmcnt(0)
	v_and_b32_e32 v39, 0xffff0000, v137
	v_lshlrev_b32_e32 v40, 16, v138
	v_and_b32_e32 v41, 0xffff0000, v138
	v_lshlrev_b32_e32 v42, 16, v139
	v_and_b32_e32 v43, 0xffff0000, v139
	v_pk_add_f32 v[32:33], v[32:33], v[36:37]
	v_pk_add_f32 v[34:35], v[34:35], v[38:39]
	v_pk_add_f32 v[36:37], v[30:31], v[42:43]
	v_pk_add_f32 v[30:31], v[28:29], v[40:41]
	v_cvt_pk_bf16_f32 v28, v32, v33
	v_cvt_pk_bf16_f32 v29, v34, v35
	v_and_b32_e32 v33, 0xffff0000, v28
	v_lshlrev_b32_e32 v32, 16, v28
	v_and_b32_e32 v35, 0xffff0000, v29
	v_mul_f32_e32 v33, v33, v33
	v_cvt_pk_bf16_f32 v30, v30, v31
	v_cvt_pk_bf16_f32 v31, v36, v37
	v_lshlrev_b32_e32 v34, 16, v29
	v_fmac_f32_e32 v33, v32, v32
	v_mul_f32_e32 v32, v35, v35
	v_and_b32_e32 v37, 0xffff0000, v30
	v_and_b32_e32 v39, 0xffff0000, v31
	v_fmac_f32_e32 v32, v34, v34
	v_lshlrev_b32_e32 v36, 16, v30
	v_lshlrev_b32_e32 v38, 16, v31
	v_add_f32_e32 v32, v33, v32
	v_mul_f32_e32 v33, v37, v37
	v_mul_f32_e32 v34, v39, v39
	v_fmac_f32_e32 v33, v36, v36
	v_fmac_f32_e32 v34, v38, v38
	v_add_f32_e32 v33, v33, v34
	v_add_f32_e32 v40, v32, v33
	s_waitcnt vmcnt(14)
	v_lshlrev_b32_e32 v32, 16, v128
	v_and_b32_e32 v33, 0xffff0000, v128
	v_lshlrev_b32_e32 v34, 16, v129
	v_and_b32_e32 v35, 0xffff0000, v129
	v_lshlrev_b32_e32 v36, 16, v130
	v_and_b32_e32 v37, 0xffff0000, v130
	v_pk_add_f32 v[24:25], v[24:25], v[32:33]
	v_lshlrev_b32_e32 v38, 16, v131
	v_and_b32_e32 v39, 0xffff0000, v131
	v_pk_add_f32 v[26:27], v[26:27], v[34:35]
	v_pk_add_f32 v[20:21], v[20:21], v[36:37]
	v_cvt_pk_bf16_f32 v24, v24, v25
	v_pk_add_f32 v[22:23], v[22:23], v[38:39]
	v_cvt_pk_bf16_f32 v25, v26, v27
	v_cvt_pk_bf16_f32 v26, v20, v21
	v_and_b32_e32 v21, 0xffff0000, v24
	v_cvt_pk_bf16_f32 v27, v22, v23
	v_lshlrev_b32_e32 v20, 16, v24
	v_and_b32_e32 v23, 0xffff0000, v25
	v_mul_f32_e32 v21, v21, v21
	v_lshlrev_b32_e32 v22, 16, v25
	v_fmac_f32_e32 v21, v20, v20
	v_mul_f32_e32 v20, v23, v23
	v_and_b32_e32 v33, 0xffff0000, v26
	v_and_b32_e32 v35, 0xffff0000, v27
	v_fmac_f32_e32 v20, v22, v22
	v_lshlrev_b32_e32 v32, 16, v26
	v_lshlrev_b32_e32 v34, 16, v27
	v_add_f32_e32 v20, v21, v20
	v_mul_f32_e32 v21, v33, v33
	v_mul_f32_e32 v22, v35, v35
	v_fmac_f32_e32 v21, v32, v32
	v_fmac_f32_e32 v22, v34, v34
	v_add_f32_e32 v21, v21, v22
	v_add_f32_e32 v20, v20, v21
	v_add_f32_e32 v22, v40, v20
	v_mov_b32_e32 v23, v22
	s_nop 3
	v_permlane16_swap_b32_e32 v22, v23
	s_nop 1
	v_add_u32_e32 v20, 0xa0, v216
	v_ashrrev_i32_e32 v21, 31, v20
	v_lshlrev_b64 v[32:33], 11, v[20:21]
	v_lshl_add_u64 v[32:33], s[14:15], 0, v[32:33]
	s_waitcnt lgkmcnt(0)
	v_add_f32_e32 v22, v22, v23
	v_mov_b32_e32 v23, v22
	s_nop 3
	v_permlane32_swap_b32_e32 v22, v23
	s_nop 1
	v_lshl_add_u64 v[32:33], v[214:215], 1, v[32:33]
	global_store_dwordx4 v[32:33], v[28:31], off
	global_store_dwordx4 v[32:33], v[24:27], off offset:256
	s_and_saveexec_b64 s[4:5], vcc
	s_cbranch_execz .LBB0_1135
	v_lshlrev_b64 v[20:21], 6, v[20:21]
	v_lshl_add_u64 v[20:21], s[18:19], 0, v[20:21]
	v_lshl_add_u64 v[20:21], s[44:45], 2, v[20:21]
	s_lshl_b32 s56, s53, 2
	v_lshl_add_u64 v[20:21], v[20:21], 0, s[56:57]
	s_waitcnt lgkmcnt(0)
	v_add_f32_e32 v22, v22, v23
	global_store_dword v[20:21], v22, off
.LBB0_1135:
	s_or_b64 exec, exec, s[4:5]
	s_waitcnt vmcnt(15)
	v_lshlrev_b32_e32 v20, 16, v116
	v_and_b32_e32 v21, 0xffff0000, v116
	v_lshlrev_b32_e32 v22, 16, v117
	s_waitcnt lgkmcnt(0)
	v_and_b32_e32 v23, 0xffff0000, v117
	v_lshlrev_b32_e32 v24, 16, v118
	v_and_b32_e32 v25, 0xffff0000, v118
	v_lshlrev_b32_e32 v26, 16, v119
	v_and_b32_e32 v27, 0xffff0000, v119
	v_pk_add_f32 v[16:17], v[16:17], v[20:21]
	v_pk_add_f32 v[18:19], v[18:19], v[22:23]
	v_pk_add_f32 v[20:21], v[14:15], v[26:27]
	v_pk_add_f32 v[14:15], v[12:13], v[24:25]
	v_cvt_pk_bf16_f32 v12, v16, v17
	v_cvt_pk_bf16_f32 v13, v18, v19
	v_and_b32_e32 v17, 0xffff0000, v12
	v_lshlrev_b32_e32 v16, 16, v12
	v_and_b32_e32 v19, 0xffff0000, v13
	v_mul_f32_e32 v17, v17, v17
	v_cvt_pk_bf16_f32 v14, v14, v15
	v_cvt_pk_bf16_f32 v15, v20, v21
	v_lshlrev_b32_e32 v18, 16, v13
	v_fmac_f32_e32 v17, v16, v16
	v_mul_f32_e32 v16, v19, v19
	v_and_b32_e32 v21, 0xffff0000, v14
	v_and_b32_e32 v23, 0xffff0000, v15
	v_fmac_f32_e32 v16, v18, v18
	v_lshlrev_b32_e32 v20, 16, v14
	v_lshlrev_b32_e32 v22, 16, v15
	v_add_f32_e32 v16, v17, v16
	v_mul_f32_e32 v17, v21, v21
	v_mul_f32_e32 v18, v23, v23
	v_fmac_f32_e32 v17, v20, v20
	v_fmac_f32_e32 v18, v22, v22
	v_add_f32_e32 v17, v17, v18
	v_add_f32_e32 v24, v16, v17
	s_waitcnt vmcnt(14)
	v_lshlrev_b32_e32 v16, 16, v108
	v_and_b32_e32 v17, 0xffff0000, v108
	v_lshlrev_b32_e32 v18, 16, v109
	v_and_b32_e32 v19, 0xffff0000, v109
	v_lshlrev_b32_e32 v20, 16, v110
	v_and_b32_e32 v21, 0xffff0000, v110
	v_pk_add_f32 v[8:9], v[8:9], v[16:17]
	v_lshlrev_b32_e32 v22, 16, v111
	v_and_b32_e32 v23, 0xffff0000, v111
	v_pk_add_f32 v[10:11], v[10:11], v[18:19]
	v_pk_add_f32 v[4:5], v[4:5], v[20:21]
	v_cvt_pk_bf16_f32 v8, v8, v9
	v_pk_add_f32 v[6:7], v[6:7], v[22:23]
	v_cvt_pk_bf16_f32 v9, v10, v11
	v_cvt_pk_bf16_f32 v10, v4, v5
	v_and_b32_e32 v5, 0xffff0000, v8
	v_cvt_pk_bf16_f32 v11, v6, v7
	v_lshlrev_b32_e32 v4, 16, v8
	v_and_b32_e32 v7, 0xffff0000, v9
	v_mul_f32_e32 v5, v5, v5
	v_lshlrev_b32_e32 v6, 16, v9
	v_fmac_f32_e32 v5, v4, v4
	v_mul_f32_e32 v4, v7, v7
	v_and_b32_e32 v17, 0xffff0000, v10
	v_and_b32_e32 v19, 0xffff0000, v11
	v_fmac_f32_e32 v4, v6, v6
	v_lshlrev_b32_e32 v16, 16, v10
	v_lshlrev_b32_e32 v18, 16, v11
	v_add_f32_e32 v4, v5, v4
	v_mul_f32_e32 v5, v17, v17
	v_mul_f32_e32 v6, v19, v19
	v_fmac_f32_e32 v5, v16, v16
	v_fmac_f32_e32 v6, v18, v18
	v_add_f32_e32 v5, v5, v6
	v_add_f32_e32 v4, v4, v5
	v_add_f32_e32 v6, v24, v4
	v_mov_b32_e32 v7, v6
	s_nop 3
	v_permlane16_swap_b32_e32 v6, v7
	s_nop 1
	v_add_u32_e32 v4, 0xb0, v216
	v_ashrrev_i32_e32 v5, 31, v4
	v_lshlrev_b64 v[16:17], 11, v[4:5]
	v_lshl_add_u64 v[16:17], s[14:15], 0, v[16:17]
	s_waitcnt lgkmcnt(0)
	v_add_f32_e32 v6, v6, v7
	v_mov_b32_e32 v7, v6
	s_nop 3
	v_permlane32_swap_b32_e32 v6, v7
	s_nop 1
	v_lshl_add_u64 v[16:17], v[214:215], 1, v[16:17]
	global_store_dwordx4 v[16:17], v[12:15], off
	global_store_dwordx4 v[16:17], v[8:11], off offset:256
	s_and_saveexec_b64 s[4:5], vcc
	s_cbranch_execz .LBB0_1137
	v_lshlrev_b64 v[4:5], 6, v[4:5]
	v_lshl_add_u64 v[4:5], s[18:19], 0, v[4:5]
	v_lshl_add_u64 v[4:5], s[44:45], 2, v[4:5]
	s_lshl_b32 s56, s53, 2
	v_lshl_add_u64 v[4:5], v[4:5], 0, s[56:57]
	s_waitcnt lgkmcnt(0)
	v_add_f32_e32 v6, v6, v7
	global_store_dword v[4:5], v6, off
